# static s_setprio 1 for waves 4-7 for the whole kernel (set once at entry)
# speedup vs baseline: 1.0032x; 1.0032x over previous
; #define LAS __attribute__((address_space(3)))
; __global__ void __launch_bounds__(NTHR, 2) k_fused(Params p) {
;     extern __shared__ __attribute__((aligned(16))) unsigned char smem[];
;     LAS unsigned char* lds = (LAS unsigned char*)smem;
;     const int wvid = __builtin_amdgcn_readfirstlane((int)threadIdx.x >> 6);
;     volatile LAS unsigned* st = (volatile LAS unsigned*)(lds + LDS_BYTES - 16);
;     if (threadIdx.x == 0) { st[0] = 0u; st[1] = 0u; st[2] = 0u; st[3] = 0u; }
;     __syncthreads();
;     (void)xcd_barrier_post((unsigned*)(p.ws + WS_CTL) + CW_BAR, st);
_Z7k_fused6Params:
	s_load_dwordx2 s[66:67], s[0:1], 0x130
	s_load_dwordx4 s[4:7], s[0:1], 0x120
	s_mov_b32 s65, s2
	v_readfirstlane_b32 s74, v0
	s_cmp_lt_u32 s74, 0x100
	s_cbranch_scc1 .Lprio_skip
	s_setprio 1
.Lprio_skip:
	v_cmp_eq_u32_e64 s[72:73], 0, v0
	s_waitcnt lgkmcnt(0)
	v_writelane_b32 v253, s4, 0
	s_nop 1
	v_writelane_b32 v253, s5, 1
	v_writelane_b32 v253, s6, 2
	v_writelane_b32 v253, s7, 3
	s_load_dwordx8 s[4:11], s[0:1], 0x100
	s_waitcnt lgkmcnt(0)
	v_writelane_b32 v253, s4, 4
	s_nop 1
	v_writelane_b32 v253, s5, 5
	v_writelane_b32 v253, s6, 6
	v_writelane_b32 v253, s7, 7
	v_writelane_b32 v253, s8, 8
	v_writelane_b32 v253, s9, 9
	v_writelane_b32 v253, s10, 10
	v_writelane_b32 v253, s11, 11
	s_and_saveexec_b64 s[2:3], s[72:73]
	s_cbranch_execz .LBB0_2
	s_add_i32 s4, 0, 0x25ff0
	v_mov_b32_e32 v0, 0
	v_mov_b32_e32 v1, s4
	s_add_i32 s4, 0, 0x25ff4
	ds_write_b32 v1, v0
	v_mov_b32_e32 v1, s4
	s_add_i32 s4, 0, 0x25ff8
	ds_write_b32 v1, v0
	v_mov_b32_e32 v1, s4
	s_add_i32 s4, 0, 0x25ffc
	ds_write_b32 v1, v0
	v_mov_b32_e32 v1, s4
	ds_write_b32 v1, v0
